# tail top-4 selection: exec-masked compare/select stages rewritten branch-free (v_cmp + s_or + v_cndmask), same tie-break
# baseline (speedup 1.0000x reference)
; DI int shfl_src(int x, int src_lane) { return __builtin_amdgcn_ds_bpermute(src_lane << 2, x); }
; DI void phase_tail(const Frame& F, int l) {
;     ...
;             for (int w = 0; w < 8; ++w) mylogit += Pz[(w * 32 + tkl) * 32 + r];
;             float tv[4]; int tix[4];
; #pragma unroll
;             for (int k = 0; k < 4; ++k) { float v = mylogit; int idx = r;
; #pragma unroll
;                 for (int st = 0; st < 5; ++st) { float ov; int oi;
;                     if (st == 0) { ov = __builtin_bit_cast(float, __builtin_amdgcn_update_dpp(0, __builtin_bit_cast(int, v), 0xB1, 0xf, 0xf, true)); oi = __builtin_amdgcn_update_dpp(0, idx, 0xB1, 0xf, 0xf, true); }
;                     else if (st == 1) { ov = __builtin_bit_cast(float, __builtin_amdgcn_update_dpp(0, __builtin_bit_cast(int, v), 0x4E, 0xf, 0xf, true)); oi = __builtin_amdgcn_update_dpp(0, idx, 0x4E, 0xf, 0xf, true); }
;                     else if (st == 2) { ov = __builtin_bit_cast(float, __builtin_amdgcn_update_dpp(0, __builtin_bit_cast(int, v), 0x141, 0xf, 0xf, true)); oi = __builtin_amdgcn_update_dpp(0, idx, 0x141, 0xf, 0xf, true); }
;                     else if (st == 3) { ov = __builtin_bit_cast(float, __builtin_amdgcn_update_dpp(0, __builtin_bit_cast(int, v), 0x140, 0xf, 0xf, true)); oi = __builtin_amdgcn_update_dpp(0, idx, 0x140, 0xf, 0xf, true); }
;                     else { ov = __builtin_bit_cast(float, shfl_src(__builtin_bit_cast(int, v), F.lane ^ 16)); oi = shfl_src(idx, F.lane ^ 16); }
;                     if (ov > v || (ov == v && oi < idx)) { v = ov; idx = oi; } }
;                 tv[k] = v; tix[k] = idx; if (r == idx) mylogit = neg_big; }
.LBB0_963:
	v_or_b32_e32 v0, s2, v138
	v_lshl_add_u32 v1, v0, 7, v137
	ds_read2st64_b32 v[2:3], v1 offset1:16
	ds_read2st64_b32 v[100:101], v1 offset0:32 offset1:48
	ds_read2st64_b32 v[102:103], v1 offset0:64 offset1:80
	ds_read2st64_b32 v[104:105], v1 offset0:96 offset1:112
	s_mov_b32 s70, 0xffff
	s_mov_b32 s71, 0xffff
	v_mov_b32_dpp v6, v67 quad_perm:[1,0,3,2] row_mask:0xf bank_mask:0xf bound_ctrl:1
	s_waitcnt lgkmcnt(3)
	v_add_f32_e32 v2, v135, v2
	v_add_f32_e32 v4, v2, v3
	s_waitcnt lgkmcnt(2)
	v_add_f32_e32 v2, v4, v100
	v_add_f32_e32 v4, v2, v101
	s_waitcnt lgkmcnt(1)
	v_add_f32_e32 v2, v4, v102
	v_add_f32_e32 v4, v2, v103
	s_waitcnt lgkmcnt(0)
	v_add_f32_e32 v1, v4, v104
	v_add_f32_e32 v3, v1, v105
	s_nop 1
	v_mov_b32_dpp v4, v3 quad_perm:[1,0,3,2] row_mask:0xf bank_mask:0xf bound_ctrl:1
	v_cmp_lt_f32_e64 s[4:5], v3, v4
	v_cmp_eq_f32_e32 vcc, v3, v4
	v_cmp_lt_i32_e64 s[46:47], v6, v67
	s_and_b64 s[12:13], vcc, s[46:47]
	s_or_b64 s[4:5], s[4:5], s[12:13]
	v_mov_b32_e32 v5, v3
	v_mov_b32_e32 v2, v3
	v_mov_b32_e32 v1, v67
	v_cndmask_b32_e64 v5, v5, v4, s[4:5]
	v_cndmask_b32_e64 v2, v2, v4, s[4:5]
	v_cndmask_b32_e64 v1, v1, v6, s[4:5]
	s_nop 1
	v_mov_b32_dpp v4, v5 quad_perm:[2,3,0,1] row_mask:0xf bank_mask:0xf bound_ctrl:1
	v_mov_b32_dpp v6, v1 quad_perm:[2,3,0,1] row_mask:0xf bank_mask:0xf bound_ctrl:1
	v_cmp_lt_f32_e64 s[4:5], v2, v4
	v_cmp_eq_f32_e32 vcc, v2, v4
	v_cmp_lt_i32_e64 s[46:47], v6, v1
	s_and_b64 s[12:13], vcc, s[46:47]
	s_or_b64 s[4:5], s[4:5], s[12:13]
	v_cndmask_b32_e64 v5, v5, v4, s[4:5]
	v_cndmask_b32_e64 v2, v2, v4, s[4:5]
	v_cndmask_b32_e64 v1, v1, v6, s[4:5]
	s_nop 1
	v_mov_b32_dpp v4, v5 row_half_mirror row_mask:0xf bank_mask:0xf bound_ctrl:1
	v_mov_b32_dpp v6, v1 row_half_mirror row_mask:0xf bank_mask:0xf bound_ctrl:1
	v_cmp_lt_f32_e64 s[4:5], v2, v4
	v_cmp_eq_f32_e32 vcc, v2, v4
	v_cmp_lt_i32_e64 s[46:47], v6, v1
	s_and_b64 s[12:13], vcc, s[46:47]
	s_or_b64 s[4:5], s[4:5], s[12:13]
	v_cndmask_b32_e64 v5, v5, v4, s[4:5]
	v_cndmask_b32_e64 v2, v2, v4, s[4:5]
	v_cndmask_b32_e64 v1, v1, v6, s[4:5]
	s_nop 1
	v_mov_b32_dpp v4, v5 row_mirror row_mask:0xf bank_mask:0xf bound_ctrl:1
	v_mov_b32_dpp v6, v1 row_mirror row_mask:0xf bank_mask:0xf bound_ctrl:1
	v_cmp_lt_f32_e64 s[4:5], v2, v4
	v_cmp_eq_f32_e32 vcc, v2, v4
	v_cmp_lt_i32_e64 s[46:47], v6, v1
	s_and_b64 s[12:13], vcc, s[46:47]
	s_or_b64 s[4:5], s[4:5], s[12:13]
	v_cndmask_b32_e64 v5, v5, v4, s[4:5]
	v_cndmask_b32_e64 v2, v2, v4, s[4:5]
	v_cndmask_b32_e64 v1, v1, v6, s[4:5]
	v_mov_b32_e32 v106, v5
	v_mov_b32_e32 v107, v1
	v_mov_b32_e32 v108, v5
	v_mov_b32_e32 v109, v1
	s_nop 1
	v_permlane16_swap_b32_e32 v106, v108
	v_permlane16_swap_b32_e32 v107, v109
	v_cndmask_b32_e64 v5, v106, v108, s[70:71]
	v_cndmask_b32_e64 v4, v107, v109, s[70:71]
	s_waitcnt lgkmcnt(1)
	v_cmp_lt_f32_e64 s[4:5], v2, v5
	v_cmp_eq_f32_e32 vcc, v2, v5
	s_waitcnt lgkmcnt(0)
	v_cmp_lt_i32_e64 s[46:47], v4, v1
	s_and_b64 s[12:13], vcc, s[46:47]
	s_or_b64 s[4:5], s[4:5], s[12:13]
	v_cndmask_b32_e64 v2, v2, v5, s[4:5]
	v_cndmask_b32_e64 v1, v1, v4, s[4:5]
	s_nop 1
	v_cmp_eq_u32_e32 vcc, v67, v1
	v_mov_b32_dpp v8, v67 quad_perm:[1,0,3,2] row_mask:0xf bank_mask:0xf bound_ctrl:1
	s_nop 0
	v_cndmask_b32_e32 v5, v3, v136, vcc
	s_nop 1
	v_mov_b32_dpp v7, v5 quad_perm:[1,0,3,2] row_mask:0xf bank_mask:0xf bound_ctrl:1
	v_cmp_lt_f32_e64 s[4:5], v5, v7
	v_cmp_eq_f32_e32 vcc, v5, v7
	v_cmp_lt_i32_e64 s[46:47], v8, v67
	s_and_b64 s[12:13], vcc, s[46:47]
	s_or_b64 s[4:5], s[4:5], s[12:13]
	v_mov_b32_e32 v6, v5
	s_waitcnt lgkmcnt(0)
	v_mov_b32_e32 v4, v5
	v_mov_b32_e32 v3, v67
	v_cndmask_b32_e64 v6, v6, v7, s[4:5]
	v_cndmask_b32_e64 v4, v4, v7, s[4:5]
	v_cndmask_b32_e64 v3, v3, v8, s[4:5]
	s_nop 1
	v_mov_b32_dpp v7, v6 quad_perm:[2,3,0,1] row_mask:0xf bank_mask:0xf bound_ctrl:1
	v_mov_b32_dpp v8, v3 quad_perm:[2,3,0,1] row_mask:0xf bank_mask:0xf bound_ctrl:1
	v_cmp_lt_f32_e64 s[4:5], v4, v7
	v_cmp_eq_f32_e32 vcc, v4, v7
	v_cmp_lt_i32_e64 s[46:47], v8, v3
	s_and_b64 s[12:13], vcc, s[46:47]
	s_or_b64 s[4:5], s[4:5], s[12:13]
	v_cndmask_b32_e64 v6, v6, v7, s[4:5]
	v_cndmask_b32_e64 v4, v4, v7, s[4:5]
	v_cndmask_b32_e64 v3, v3, v8, s[4:5]
	s_nop 1
	v_mov_b32_dpp v7, v6 row_half_mirror row_mask:0xf bank_mask:0xf bound_ctrl:1
	v_mov_b32_dpp v8, v3 row_half_mirror row_mask:0xf bank_mask:0xf bound_ctrl:1
	v_cmp_lt_f32_e64 s[4:5], v4, v7
	v_cmp_eq_f32_e32 vcc, v4, v7
	v_cmp_lt_i32_e64 s[46:47], v8, v3
	s_and_b64 s[12:13], vcc, s[46:47]
	s_or_b64 s[4:5], s[4:5], s[12:13]
	v_cndmask_b32_e64 v6, v6, v7, s[4:5]
	v_cndmask_b32_e64 v4, v4, v7, s[4:5]
	v_cndmask_b32_e64 v3, v3, v8, s[4:5]
	s_nop 1
	v_mov_b32_dpp v7, v6 row_mirror row_mask:0xf bank_mask:0xf bound_ctrl:1
	v_mov_b32_dpp v8, v3 row_mirror row_mask:0xf bank_mask:0xf bound_ctrl:1
	v_cmp_lt_f32_e64 s[4:5], v4, v7
	v_cmp_eq_f32_e32 vcc, v4, v7
	v_cmp_lt_i32_e64 s[46:47], v8, v3
	s_and_b64 s[12:13], vcc, s[46:47]
	s_or_b64 s[4:5], s[4:5], s[12:13]
	v_cndmask_b32_e64 v6, v6, v7, s[4:5]
	v_cndmask_b32_e64 v4, v4, v7, s[4:5]
	v_cndmask_b32_e64 v3, v3, v8, s[4:5]
	v_mov_b32_e32 v106, v6
	v_mov_b32_e32 v107, v3
	v_mov_b32_e32 v108, v6
	v_mov_b32_e32 v109, v3
	s_nop 1
	v_permlane16_swap_b32_e32 v106, v108
	v_permlane16_swap_b32_e32 v107, v109
	v_cndmask_b32_e64 v7, v106, v108, s[70:71]
	v_cndmask_b32_e64 v6, v107, v109, s[70:71]
	s_waitcnt lgkmcnt(1)
; DI int shfl_src(int x, int src_lane) { return __builtin_amdgcn_ds_bpermute(src_lane << 2, x); }
; DI void phase_tail(const Frame& F, int l) {
;     ...
;             for (int w = 0; w < 8; ++w) mylogit += Pz[(w * 32 + tkl) * 32 + r];
;             float tv[4]; int tix[4];
; #pragma unroll
;             for (int k = 0; k < 4; ++k) { float v = mylogit; int idx = r;
; #pragma unroll
;                 for (int st = 0; st < 5; ++st) { float ov; int oi;
;                     if (st == 0) { ov = __builtin_bit_cast(float, __builtin_amdgcn_update_dpp(0, __builtin_bit_cast(int, v), 0xB1, 0xf, 0xf, true)); oi = __builtin_amdgcn_update_dpp(0, idx, 0xB1, 0xf, 0xf, true); }
;                     else if (st == 1) { ov = __builtin_bit_cast(float, __builtin_amdgcn_update_dpp(0, __builtin_bit_cast(int, v), 0x4E, 0xf, 0xf, true)); oi = __builtin_amdgcn_update_dpp(0, idx, 0x4E, 0xf, 0xf, true); }
;                     else if (st == 2) { ov = __builtin_bit_cast(float, __builtin_amdgcn_update_dpp(0, __builtin_bit_cast(int, v), 0x141, 0xf, 0xf, true)); oi = __builtin_amdgcn_update_dpp(0, idx, 0x141, 0xf, 0xf, true); }
;                     else if (st == 3) { ov = __builtin_bit_cast(float, __builtin_amdgcn_update_dpp(0, __builtin_bit_cast(int, v), 0x140, 0xf, 0xf, true)); oi = __builtin_amdgcn_update_dpp(0, idx, 0x140, 0xf, 0xf, true); }
;                     else { ov = __builtin_bit_cast(float, shfl_src(__builtin_bit_cast(int, v), F.lane ^ 16)); oi = shfl_src(idx, F.lane ^ 16); }
;                     if (ov > v || (ov == v && oi < idx)) { v = ov; idx = oi; } }
;                 tv[k] = v; tix[k] = idx; if (r == idx) mylogit = neg_big; }
	v_cmp_lt_f32_e64 s[4:5], v4, v7
	v_cmp_eq_f32_e32 vcc, v4, v7
	s_waitcnt lgkmcnt(0)
	v_cmp_lt_i32_e64 s[46:47], v6, v3
	s_and_b64 s[12:13], vcc, s[46:47]
	s_or_b64 s[4:5], s[4:5], s[12:13]
	v_cndmask_b32_e64 v4, v4, v7, s[4:5]
	v_cndmask_b32_e64 v3, v3, v6, s[4:5]
	s_nop 1
	v_cmp_eq_u32_e32 vcc, v67, v3
	v_mov_b32_dpp v10, v67 quad_perm:[1,0,3,2] row_mask:0xf bank_mask:0xf bound_ctrl:1
	s_nop 0
	v_cndmask_b32_e32 v7, v5, v136, vcc
	s_nop 1
	v_mov_b32_dpp v9, v7 quad_perm:[1,0,3,2] row_mask:0xf bank_mask:0xf bound_ctrl:1
	v_cmp_lt_f32_e64 s[4:5], v7, v9
	v_cmp_eq_f32_e32 vcc, v7, v9
	v_cmp_lt_i32_e64 s[46:47], v10, v67
	s_and_b64 s[12:13], vcc, s[46:47]
	s_or_b64 s[4:5], s[4:5], s[12:13]
	v_mov_b32_e32 v8, v7
	s_waitcnt lgkmcnt(0)
	v_mov_b32_e32 v6, v7
	v_mov_b32_e32 v5, v67
	v_cndmask_b32_e64 v8, v8, v9, s[4:5]
	v_cndmask_b32_e64 v6, v6, v9, s[4:5]
	v_cndmask_b32_e64 v5, v5, v10, s[4:5]
	s_nop 1
	v_mov_b32_dpp v9, v8 quad_perm:[2,3,0,1] row_mask:0xf bank_mask:0xf bound_ctrl:1
	v_mov_b32_dpp v10, v5 quad_perm:[2,3,0,1] row_mask:0xf bank_mask:0xf bound_ctrl:1
	v_cmp_lt_f32_e64 s[4:5], v6, v9
	v_cmp_eq_f32_e32 vcc, v6, v9
	v_cmp_lt_i32_e64 s[46:47], v10, v5
	s_and_b64 s[12:13], vcc, s[46:47]
	s_or_b64 s[4:5], s[4:5], s[12:13]
	v_cndmask_b32_e64 v8, v8, v9, s[4:5]
	v_cndmask_b32_e64 v6, v6, v9, s[4:5]
	v_cndmask_b32_e64 v5, v5, v10, s[4:5]
	s_nop 1
	v_mov_b32_dpp v9, v8 row_half_mirror row_mask:0xf bank_mask:0xf bound_ctrl:1
	v_mov_b32_dpp v10, v5 row_half_mirror row_mask:0xf bank_mask:0xf bound_ctrl:1
	v_cmp_lt_f32_e64 s[4:5], v6, v9
	v_cmp_eq_f32_e32 vcc, v6, v9
	v_cmp_lt_i32_e64 s[46:47], v10, v5
	s_and_b64 s[12:13], vcc, s[46:47]
	s_or_b64 s[4:5], s[4:5], s[12:13]
	v_cndmask_b32_e64 v8, v8, v9, s[4:5]
	v_cndmask_b32_e64 v6, v6, v9, s[4:5]
	v_cndmask_b32_e64 v5, v5, v10, s[4:5]
	s_nop 1
	v_mov_b32_dpp v9, v8 row_mirror row_mask:0xf bank_mask:0xf bound_ctrl:1
	v_mov_b32_dpp v10, v5 row_mirror row_mask:0xf bank_mask:0xf bound_ctrl:1
	v_cmp_lt_f32_e64 s[4:5], v6, v9
	v_cmp_eq_f32_e32 vcc, v6, v9
	v_cmp_lt_i32_e64 s[46:47], v10, v5
	s_and_b64 s[12:13], vcc, s[46:47]
	s_or_b64 s[4:5], s[4:5], s[12:13]
	v_cndmask_b32_e64 v8, v8, v9, s[4:5]
	v_cndmask_b32_e64 v6, v6, v9, s[4:5]
	v_cndmask_b32_e64 v5, v5, v10, s[4:5]
	v_mov_b32_e32 v106, v8
	v_mov_b32_e32 v107, v5
	v_mov_b32_e32 v108, v8
	v_mov_b32_e32 v109, v5
	s_nop 1
	v_permlane16_swap_b32_e32 v106, v108
	v_permlane16_swap_b32_e32 v107, v109
	v_cndmask_b32_e64 v9, v106, v108, s[70:71]
	v_cndmask_b32_e64 v8, v107, v109, s[70:71]
	s_waitcnt lgkmcnt(1)
	v_cmp_lt_f32_e64 s[4:5], v6, v9
	v_cmp_eq_f32_e32 vcc, v6, v9
	s_waitcnt lgkmcnt(0)
	v_cmp_lt_i32_e64 s[46:47], v8, v5
	s_and_b64 s[12:13], vcc, s[46:47]
	s_or_b64 s[4:5], s[4:5], s[12:13]
	v_cndmask_b32_e64 v6, v6, v9, s[4:5]
	v_cndmask_b32_e64 v5, v5, v8, s[4:5]
	s_nop 1
	v_cmp_eq_u32_e32 vcc, v67, v5
	v_mov_b32_dpp v9, v67 quad_perm:[1,0,3,2] row_mask:0xf bank_mask:0xf bound_ctrl:1
	s_nop 0
	v_cndmask_b32_e32 v7, v7, v136, vcc
	s_nop 1
	v_mov_b32_dpp v10, v7 quad_perm:[1,0,3,2] row_mask:0xf bank_mask:0xf bound_ctrl:1
	v_cmp_lt_f32_e64 s[4:5], v7, v10
	v_cmp_eq_f32_e32 vcc, v7, v10
	v_cmp_lt_i32_e64 s[46:47], v9, v67
	s_and_b64 s[12:13], vcc, s[46:47]
	s_or_b64 s[4:5], s[4:5], s[12:13]
	s_waitcnt lgkmcnt(0)
	v_mov_b32_e32 v8, v67
	v_cndmask_b32_e64 v7, v7, v10, s[4:5]
	v_cndmask_b32_e64 v8, v8, v9, s[4:5]
	s_nop 1
	v_mov_b32_dpp v10, v7 quad_perm:[2,3,0,1] row_mask:0xf bank_mask:0xf bound_ctrl:1
	v_mov_b32_dpp v9, v8 quad_perm:[2,3,0,1] row_mask:0xf bank_mask:0xf bound_ctrl:1
	v_cmp_lt_f32_e64 s[4:5], v7, v10
	v_cmp_eq_f32_e32 vcc, v7, v10
	v_cmp_lt_i32_e64 s[46:47], v9, v8
	s_and_b64 s[12:13], vcc, s[46:47]
	s_or_b64 s[4:5], s[4:5], s[12:13]
	v_cndmask_b32_e64 v7, v7, v10, s[4:5]
	v_cndmask_b32_e64 v8, v8, v9, s[4:5]
	s_nop 1
	v_mov_b32_dpp v10, v7 row_half_mirror row_mask:0xf bank_mask:0xf bound_ctrl:1
	v_mov_b32_dpp v9, v8 row_half_mirror row_mask:0xf bank_mask:0xf bound_ctrl:1
	v_cmp_lt_f32_e64 s[4:5], v7, v10
	v_cmp_eq_f32_e32 vcc, v7, v10
	v_cmp_lt_i32_e64 s[46:47], v9, v8
	s_and_b64 s[12:13], vcc, s[46:47]
	s_or_b64 s[4:5], s[4:5], s[12:13]
	v_cndmask_b32_e64 v7, v7, v10, s[4:5]
	v_cndmask_b32_e64 v8, v8, v9, s[4:5]
	s_nop 1
	v_mov_b32_dpp v10, v7 row_mirror row_mask:0xf bank_mask:0xf bound_ctrl:1
	v_mov_b32_dpp v9, v8 row_mirror row_mask:0xf bank_mask:0xf bound_ctrl:1
	v_cmp_lt_f32_e64 s[4:5], v7, v10
	v_cmp_eq_f32_e32 vcc, v7, v10
	v_cmp_lt_i32_e64 s[46:47], v9, v8
	s_and_b64 s[12:13], vcc, s[46:47]
	s_or_b64 s[4:5], s[4:5], s[12:13]
	v_cndmask_b32_e64 v7, v7, v10, s[4:5]
	v_cndmask_b32_e64 v8, v8, v9, s[4:5]
	v_mov_b32_e32 v106, v7
	v_mov_b32_e32 v107, v8
	v_mov_b32_e32 v108, v7
	v_mov_b32_e32 v109, v8
	s_nop 1
	v_permlane16_swap_b32_e32 v106, v108
	v_permlane16_swap_b32_e32 v107, v109
	v_cndmask_b32_e64 v10, v106, v108, s[70:71]
	v_cndmask_b32_e64 v9, v107, v109, s[70:71]
	s_waitcnt lgkmcnt(1)
	v_cmp_lt_f32_e64 s[4:5], v7, v10
	v_cmp_nlt_f32_e32 vcc, v7, v10
	s_and_saveexec_b64 s[6:7], vcc
	s_cbranch_execnz .LBB0_1042
	s_or_b64 exec, exec, s[6:7]
	s_and_saveexec_b64 s[6:7], s[4:5]
	s_cbranch_execnz .LBB0_1043
